# in-proj only: next unit row-statistics loads hoisted to the epilogue start
# baseline (speedup 1.0000x reference)
; #define LAS __attribute__((address_space(3)))
;     EPI_NOMID
;     __device__ __forceinline__ void begin(const Unit& u, int ui, int tid, LAS unsigned char* lds) const { if (tid < 256) rtab_put(lds, ui, tid, rstd_part16(SSQ + (size_t)(u.pm * 256 + tid) * 16, 1.f / DM), 0.f); }
.LBB0_352:
	s_and_b64 vcc, exec, s[10:11]
	s_cbranch_vccnz .Lpf_in_skip
	s_and_saveexec_b64 s[16:17], s[8:9]
	v_lshl_add_u32 v240, s79, 8, v188
	v_ashrrev_i32_e32 v241, 31, v240
	v_lshlrev_b64 v[240:241], 6, v[240:241]
	v_lshl_add_u64 v[210:211], s[28:29], 0, v[240:241]
	global_load_dwordx4 v[240:243], v[210:211], off
	global_load_dwordx4 v[244:247], v[210:211], off offset:16
	global_load_dwordx4 v[194:197], v[210:211], off offset:32
	global_load_dwordx4 v[198:201], v[210:211], off offset:48
	s_mov_b64 exec, s[16:17]

; #define LAS __attribute__((address_space(3)))
; __device__ __forceinline__ float rstd_part16(const float* p, float inv_n) { const f32x4 a = ((const f32x4*)p)[0], b = ((const f32x4*)p)[1], c = ((const f32x4*)p)[2], d = ((const f32x4*)p)[3];
;     const f32x4 s4 = (a + b) + (c + d); return 1.0f / sqrtf(((s4[0] + s4[1]) + (s4[2] + s4[3])) * inv_n + EPS); }
;     EPI_NOMID
;     __device__ __forceinline__ void begin(const Unit& u, int ui, int tid, LAS unsigned char* lds) const { if (tid < 256) rtab_put(lds, ui, tid, rstd_part16(SSQ + (size_t)(u.pm * 256 + tid) * 16, 1.f / DM), 0.f); }
.LBB0_592:
	s_and_b64 vcc, exec, s[10:11]
	s_mov_b64 s[10:11], -1
	s_cbranch_vccnz .LBB0_341
	s_and_saveexec_b64 s[12:13], s[8:9]
	s_cbranch_execz .LBB0_595
	s_mov_b32 s3, 0xf800000
	s_waitcnt vmcnt(0) lgkmcnt(0)
	v_pk_add_f32 v[4:5], v[242:243], v[246:247]
	v_pk_add_f32 v[2:3], v[240:241], v[244:245]
	v_pk_add_f32 v[6:7], v[196:197], v[200:201]
	v_pk_add_f32 v[8:9], v[194:195], v[198:199]
	v_pk_add_f32 v[4:5], v[4:5], v[6:7]
	v_pk_add_f32 v[2:3], v[2:3], v[8:9]
	s_nop 0
	v_pk_mov_b32 v[6:7], v[2:3], v[4:5] op_sel:[1,0]
	v_mov_b32_e32 v3, v5
	v_pk_add_f32 v[2:3], v[6:7], v[2:3]
	s_nop 0
	v_add_f32_e32 v0, v2, v3
	v_fmamk_f32 v0, v0, 0x3a800000, v236
	v_cmp_gt_f32_e32 vcc, s3, v0
	v_mul_f32_e32 v2, 0x4f800000, v0
	s_lshl_b32 s3, s78, 11
	v_cndmask_b32_e32 v0, v0, v2, vcc
	v_sqrt_f32_e32 v2, v0
	s_and_b32 s3, s3, 0x800
	s_add_i32 s3, s3, 0
	v_add_u32_e32 v3, -1, v2
	v_fma_f32 v4, -v3, v2, v0
	v_cmp_ge_f32_e64 s[10:11], 0, v4
	v_add_u32_e32 v4, 1, v2
	s_nop 0
	v_cndmask_b32_e64 v3, v2, v3, s[10:11]
	v_fma_f32 v2, -v4, v2, v0
	v_cmp_lt_f32_e64 s[10:11], 0, v2
	s_nop 1
	v_cndmask_b32_e64 v2, v3, v4, s[10:11]
	v_mul_f32_e32 v3, 0x37800000, v2
	v_cndmask_b32_e32 v2, v2, v3, vcc
	v_cmp_class_f32_e32 vcc, v0, v251
	s_nop 1
	v_cndmask_b32_e32 v0, v2, v0, vcc
	v_div_scale_f32 v2, s[6:7], v0, v0, 1.0
	v_rcp_f32_e32 v3, v2
	s_nop 0
	v_fma_f32 v4, -v2, v3, 1.0
	v_fmac_f32_e32 v3, v4, v3
	v_div_scale_f32 v4, vcc, 1.0, v0, 1.0
	v_mul_f32_e32 v5, v4, v3
	v_fma_f32 v6, -v2, v5, v4
	v_fmac_f32_e32 v5, v6, v3
	v_fma_f32 v2, -v2, v5, v4
	v_div_fmas_f32 v2, v2, v3, v5
	v_div_fixup_f32 v0, v2, v0, 1.0
	v_mov_b32_e32 v2, v188
	s_nop 0
	v_lshl_add_u32 v2, v2, 3, s3
	v_add_u32_e32 v2, 0x22400, v2
	ds_write_b64 v2, v[0:1]
